# baseline (speedup 1.0000x reference)
.LBB0_155:
	v_mov_b32_e32 v75, s24
	s_load_dword s13, s[0:1], 0x40
	ds_read_b128 v[76:79], v75
	v_mov_b32_e32 v69, 0
	s_waitcnt lgkmcnt(0)
	s_ashr_i32 s18, s13, 31
	s_lshl_b64 s[4:5], s[16:17], 11
	v_lshl_add_u64 v[72:73], s[8:9], 0, v[68:69]
	v_lshl_add_u64 v[70:71], s[10:11], 0, v[68:69]
	v_readfirstlane_b32 s8, v76
	v_mov_b32_e32 v36, 0
	v_mov_b32_e32 v37, 0
	v_mov_b32_e32 v38, 0
	v_mov_b32_e32 v39, 0
	v_mov_b32_e32 v4, 0
	v_mov_b32_e32 v5, 0
	v_mov_b32_e32 v6, 0
	v_mov_b32_e32 v7, 0
	s_and_saveexec_b64 s[6:7], s[2:3]
	s_cbranch_execz .LBB0_157
	s_ashr_i32 s9, s8, 31
	s_add_u32 s8, s4, s8
	s_addc_u32 s9, s5, s9
	s_mul_i32 s10, s8, s18
	s_mul_hi_u32 s11, s8, s13
	s_add_i32 s10, s11, s10
	s_mul_i32 s9, s9, s13
	s_add_i32 s9, s10, s9
	s_mul_i32 s8, s8, s13
	s_lshl_b64 s[8:9], s[8:9], 1
	v_lshl_add_u64 v[4:5], v[72:73], 0, s[8:9]
	global_load_dwordx4 v[36:39], v[4:5], off
	v_lshl_add_u64 v[4:5], v[70:71], 0, s[8:9]
	global_load_dwordx4 v[4:7], v[4:5], off
.LBB0_157:
	s_or_b64 exec, exec, s[6:7]
	v_mov_b32_e32 v45, 0
	v_mov_b32_e32 v46, 0
	v_mov_b32_e32 v47, 0
	v_mov_b32_e32 v8, 0
	s_waitcnt lgkmcnt(0)
	v_readfirstlane_b32 s8, v77
	v_mov_b32_e32 v9, 0
	v_mov_b32_e32 v10, 0
	v_mov_b32_e32 v11, 0
	s_and_saveexec_b64 s[6:7], s[2:3]
	s_cbranch_execz .LBB0_159
	s_ashr_i32 s9, s8, 31
	s_add_u32 s8, s4, s8
	s_addc_u32 s9, s5, s9
	s_mul_i32 s10, s8, s18
	s_mul_hi_u32 s11, s8, s13
	s_add_i32 s10, s11, s10
	s_mul_i32 s9, s9, s13
	s_add_i32 s9, s10, s9
	s_mul_i32 s8, s8, s13
	s_lshl_b64 s[8:9], s[8:9], 1
	v_lshl_add_u64 v[8:9], v[72:73], 0, s[8:9]
	global_load_dwordx4 v[44:47], v[8:9], off
	v_lshl_add_u64 v[8:9], v[70:71], 0, s[8:9]
	global_load_dwordx4 v[8:11], v[8:9], off
	s_waitcnt vmcnt(1)
	v_mov_b32_e32 v69, v44
.LBB0_159:
	s_or_b64 exec, exec, s[6:7]
	v_mov_b32_e32 v40, 0
	v_mov_b32_e32 v48, 0
	v_mov_b32_e32 v49, 0
	v_mov_b32_e32 v50, 0
	s_waitcnt lgkmcnt(0)
	v_readfirstlane_b32 s8, v78
	v_mov_b32_e32 v51, 0
	v_mov_b32_e32 v12, 0
	v_mov_b32_e32 v13, 0
	v_mov_b32_e32 v14, 0
	v_mov_b32_e32 v15, 0
	s_and_saveexec_b64 s[6:7], s[2:3]
	s_cbranch_execz .LBB0_161
	s_ashr_i32 s9, s8, 31
	s_add_u32 s8, s4, s8
	s_addc_u32 s9, s5, s9
	s_mul_i32 s10, s8, s18
	s_mul_hi_u32 s11, s8, s13
	s_add_i32 s10, s11, s10
	s_mul_i32 s9, s9, s13
	s_add_i32 s9, s10, s9
	s_mul_i32 s8, s8, s13
	s_lshl_b64 s[8:9], s[8:9], 1
	v_lshl_add_u64 v[12:13], v[72:73], 0, s[8:9]
	global_load_dwordx4 v[48:51], v[12:13], off
	v_lshl_add_u64 v[12:13], v[70:71], 0, s[8:9]
	global_load_dwordx4 v[12:15], v[12:13], off
.LBB0_161:
	s_or_b64 exec, exec, s[6:7]
	v_mov_b32_e32 v41, 0
	v_mov_b32_e32 v42, 0
	v_mov_b32_e32 v43, 0
	v_mov_b32_e32 v16, 0
	s_waitcnt lgkmcnt(0)
	v_readfirstlane_b32 s8, v79
	ds_read_b128 v[76:79], v75 offset:16
	v_mov_b32_e32 v17, 0
	v_mov_b32_e32 v18, 0
	v_mov_b32_e32 v19, 0
	s_and_saveexec_b64 s[6:7], s[2:3]
	s_cbranch_execz .LBB0_163
	s_ashr_i32 s9, s8, 31
	s_add_u32 s8, s4, s8
	s_addc_u32 s9, s5, s9
	s_mul_i32 s10, s8, s18
	s_mul_hi_u32 s11, s8, s13
	s_add_i32 s10, s11, s10
	s_mul_i32 s9, s9, s13
	s_add_i32 s9, s10, s9
	s_mul_i32 s8, s8, s13
	s_lshl_b64 s[8:9], s[8:9], 1
	v_lshl_add_u64 v[16:17], v[72:73], 0, s[8:9]
	global_load_dwordx4 v[40:43], v[16:17], off
	v_lshl_add_u64 v[16:17], v[70:71], 0, s[8:9]
	global_load_dwordx4 v[16:19], v[16:17], off
.LBB0_163:
	s_or_b64 exec, exec, s[6:7]
	v_mov_b32_e32 v52, 0
	v_mov_b32_e32 v56, 0
	v_mov_b32_e32 v57, 0
	v_mov_b32_e32 v58, 0
	s_waitcnt lgkmcnt(0)
	v_readfirstlane_b32 s8, v76
	v_mov_b32_e32 v59, 0
	v_mov_b32_e32 v20, 0
	v_mov_b32_e32 v21, 0
	v_mov_b32_e32 v22, 0
	v_mov_b32_e32 v23, 0
	s_and_saveexec_b64 s[6:7], s[2:3]
	s_cbranch_execz .LBB0_165
	s_ashr_i32 s9, s8, 31
	s_add_u32 s8, s4, s8
	s_addc_u32 s9, s5, s9
	s_mul_i32 s10, s8, s18
	s_mul_hi_u32 s11, s8, s13
	s_add_i32 s10, s11, s10
	s_mul_i32 s9, s9, s13
	s_add_i32 s9, s10, s9
	s_mul_i32 s8, s8, s13
	s_lshl_b64 s[8:9], s[8:9], 1
	v_lshl_add_u64 v[20:21], v[72:73], 0, s[8:9]
	global_load_dwordx4 v[56:59], v[20:21], off
	v_lshl_add_u64 v[20:21], v[70:71], 0, s[8:9]
	global_load_dwordx4 v[20:23], v[20:21], off
.LBB0_165:
	s_or_b64 exec, exec, s[6:7]
	v_mov_b32_e32 v53, 0
	v_mov_b32_e32 v54, 0
	v_mov_b32_e32 v55, 0
	v_mov_b32_e32 v24, 0
	s_waitcnt lgkmcnt(0)
	v_readfirstlane_b32 s8, v77
	v_mov_b32_e32 v25, 0
	v_mov_b32_e32 v26, 0
	v_mov_b32_e32 v27, 0
	s_and_saveexec_b64 s[6:7], s[2:3]
	s_cbranch_execz .LBB0_167
	s_ashr_i32 s9, s8, 31
	s_add_u32 s8, s4, s8
	s_addc_u32 s9, s5, s9
	s_mul_i32 s10, s8, s18
	s_mul_hi_u32 s11, s8, s13
	s_add_i32 s10, s11, s10
	s_mul_i32 s9, s9, s13
	s_add_i32 s9, s10, s9
	s_mul_i32 s8, s8, s13
	s_lshl_b64 s[8:9], s[8:9], 1
	v_lshl_add_u64 v[24:25], v[72:73], 0, s[8:9]
	global_load_dwordx4 v[52:55], v[24:25], off
	v_lshl_add_u64 v[24:25], v[70:71], 0, s[8:9]
	global_load_dwordx4 v[24:27], v[24:25], off
.LBB0_167:
	s_or_b64 exec, exec, s[6:7]
	v_mov_b32_e32 v60, 0
	v_mov_b32_e32 v64, 0
	v_mov_b32_e32 v65, 0
	v_mov_b32_e32 v66, 0
	s_waitcnt lgkmcnt(0)
	v_readfirstlane_b32 s8, v78
	v_mov_b32_e32 v67, 0
	v_mov_b32_e32 v28, 0
	v_mov_b32_e32 v29, 0
	v_mov_b32_e32 v30, 0
	v_mov_b32_e32 v31, 0
	s_and_saveexec_b64 s[6:7], s[2:3]
	s_cbranch_execz .LBB0_169
	s_ashr_i32 s9, s8, 31
	s_add_u32 s8, s4, s8
	s_addc_u32 s9, s5, s9
	s_mul_i32 s10, s8, s18
	s_mul_hi_u32 s11, s8, s13
	s_add_i32 s10, s11, s10
	s_mul_i32 s9, s9, s13
	s_add_i32 s9, s10, s9
	s_mul_i32 s8, s8, s13
	s_lshl_b64 s[8:9], s[8:9], 1
	v_lshl_add_u64 v[28:29], v[72:73], 0, s[8:9]
	global_load_dwordx4 v[64:67], v[28:29], off
	v_lshl_add_u64 v[28:29], v[70:71], 0, s[8:9]
	global_load_dwordx4 v[28:31], v[28:29], off
.LBB0_169:
	s_or_b64 exec, exec, s[6:7]
	v_mov_b32_e32 v61, 0
	v_mov_b32_e32 v62, 0
	v_mov_b32_e32 v63, 0
	v_mov_b32_e32 v32, 0
	s_waitcnt lgkmcnt(0)
	v_readfirstlane_b32 s8, v79
	v_mov_b32_e32 v33, 0
	v_mov_b32_e32 v34, 0
	v_mov_b32_e32 v35, 0
	s_and_saveexec_b64 s[6:7], s[2:3]
	s_cbranch_execz .LBB0_171
	s_ashr_i32 s9, s8, 31
	s_add_u32 s4, s4, s8
	s_addc_u32 s5, s5, s9
	s_mul_i32 s8, s4, s18
	s_mul_hi_u32 s9, s4, s13
	s_add_i32 s8, s9, s8
	s_mul_i32 s5, s5, s13
	s_add_i32 s5, s8, s5
	s_mul_i32 s4, s4, s13
	s_lshl_b64 s[4:5], s[4:5], 1
	v_lshl_add_u64 v[32:33], v[72:73], 0, s[4:5]
	global_load_dwordx4 v[60:63], v[32:33], off
	v_lshl_add_u64 v[32:33], v[70:71], 0, s[4:5]
	global_load_dwordx4 v[32:35], v[32:33], off

	.amdhsa_kernel _Z12graph_kerneliPKfS0_S0_PKtiS2_S2_iPti
		.amdhsa_group_segment_fixed_size 128
		.amdhsa_private_segment_fixed_size 0
		.amdhsa_kernarg_size 84
		.amdhsa_user_sgpr_count 2
		.amdhsa_user_sgpr_dispatch_ptr 0
		.amdhsa_user_sgpr_queue_ptr 0
		.amdhsa_user_sgpr_kernarg_segment_ptr 1
		.amdhsa_user_sgpr_dispatch_id 0
		.amdhsa_user_sgpr_kernarg_preload_length 0
		.amdhsa_user_sgpr_kernarg_preload_offset 0
		.amdhsa_user_sgpr_private_segment_size 0
		.amdhsa_uses_dynamic_stack 0
		.amdhsa_enable_private_segment 0
		.amdhsa_system_sgpr_workgroup_id_x 1
		.amdhsa_system_sgpr_workgroup_id_y 0
		.amdhsa_system_sgpr_workgroup_id_z 0
		.amdhsa_system_sgpr_workgroup_info 0
		.amdhsa_system_vgpr_workitem_id 0
		.amdhsa_next_free_vgpr 80
		.amdhsa_next_free_sgpr 42
		.amdhsa_accum_offset 80
		.amdhsa_reserve_vcc 1
		.amdhsa_float_round_mode_32 0
		.amdhsa_float_round_mode_16_64 0
		.amdhsa_float_denorm_mode_32 3
		.amdhsa_float_denorm_mode_16_64 3
		.amdhsa_dx10_clamp 1
		.amdhsa_ieee_mode 1
		.amdhsa_fp16_overflow 0
		.amdhsa_tg_split 0
		.amdhsa_exception_fp_ieee_invalid_op 0
		.amdhsa_exception_fp_denorm_src 0
		.amdhsa_exception_fp_ieee_div_zero 0
		.amdhsa_exception_fp_ieee_overflow 0
		.amdhsa_exception_fp_ieee_underflow 0
		.amdhsa_exception_fp_ieee_inexact 0
		.amdhsa_exception_int_div_zero 0
	.end_amdhsa_kernel

amdhsa.kernels:
  - .agpr_count:     0
    .args:
      - .offset:         0
        .size:           4
        .value_kind:     by_value
      - .actual_access:  read_only
        .address_space:  global
        .offset:         8
        .size:           8
        .value_kind:     global_buffer
      - .actual_access:  read_only
        .address_space:  global
        .offset:         16
        .size:           8
        .value_kind:     global_buffer
      - .actual_access:  read_only
        .address_space:  global
        .offset:         24
        .size:           8
        .value_kind:     global_buffer
      - .actual_access:  read_only
        .address_space:  global
        .offset:         32
        .size:           8
        .value_kind:     global_buffer
      - .offset:         40
        .size:           4
        .value_kind:     by_value
      - .actual_access:  read_only
        .address_space:  global
        .offset:         48
        .size:           8
        .value_kind:     global_buffer
      - .actual_access:  read_only
        .address_space:  global
        .offset:         56
        .size:           8
        .value_kind:     global_buffer
      - .offset:         64
        .size:           4
        .value_kind:     by_value
      - .actual_access:  write_only
        .address_space:  global
        .offset:         72
        .size:           8
        .value_kind:     global_buffer
      - .offset:         80
        .size:           4
        .value_kind:     by_value
    .group_segment_fixed_size: 128
    .kernarg_segment_align: 8
    .kernarg_segment_size: 84
    .language:       OpenCL C
    .language_version:
      - 2
      - 0
    .max_flat_workgroup_size: 256
    .name:           _Z12graph_kerneliPKfS0_S0_PKtiS2_S2_iPti
    .private_segment_fixed_size: 0
    .sgpr_count:     48
    .sgpr_spill_count: 0
    .symbol:         _Z12graph_kerneliPKfS0_S0_PKtiS2_S2_iPti.kd
    .uniform_work_group_size: 1
    .uses_dynamic_stack: false
    .vgpr_count:     80
    .vgpr_spill_count: 0
    .wavefront_size: 64
  - .agpr_count:     0
    .args:
      - .offset:         0
        .size:           96
        .value_kind:     by_value
      - .offset:         96
        .size:           336
        .value_kind:     by_value
      - .offset:         432
        .size:           328
        .value_kind:     by_value
    .group_segment_fixed_size: 50688
    .kernarg_segment_align: 8
    .kernarg_segment_size: 760
    .language:       OpenCL C
    .language_version:
      - 2
      - 0
    .max_flat_workgroup_size: 512
    .name:           _Z12front_kernel9FrontArgs8PrepArgs8FragArgs
    .private_segment_fixed_size: 0
    .sgpr_count:     58
    .sgpr_spill_count: 0
    .symbol:         _Z12front_kernel9FrontArgs8PrepArgs8FragArgs.kd
    .uniform_work_group_size: 1
    .uses_dynamic_stack: false
    .vgpr_count:     80
    .vgpr_spill_count: 0
    .wavefront_size: 64
  - .agpr_count:     0
    .args:
      - .offset:         0
        .size:           144
        .value_kind:     by_value
    .group_segment_fixed_size: 131072
    .kernarg_segment_align: 8
    .kernarg_segment_size: 144
    .language:       OpenCL C
    .language_version:
      - 2
      - 0
    .max_flat_workgroup_size: 512
    .name:           _Z13gemm8p_kernel5GArgs
    .private_segment_fixed_size: 0
    .sgpr_count:     42
    .sgpr_spill_count: 0
    .symbol:         _Z13gemm8p_kernel5GArgs.kd
    .uniform_work_group_size: 1
    .uses_dynamic_stack: false
    .vgpr_count:     250
    .vgpr_spill_count: 0
    .wavefront_size: 64
  - .agpr_count:     0
    .args:
      - .actual_access:  read_only
        .address_space:  global
        .offset:         0
        .size:           8
        .value_kind:     global_buffer
      - .offset:         8
        .size:           4
        .value_kind:     by_value
      - .address_space:  global
        .offset:         16
        .size:           8
        .value_kind:     global_buffer
      - .offset:         24
        .size:           4
        .value_kind:     by_value
      - .address_space:  global
        .offset:         32
        .size:           8
        .value_kind:     global_buffer
      - .offset:         40
        .size:           4
        .value_kind:     by_value
      - .actual_access:  write_only
        .address_space:  global
        .offset:         48
        .size:           8
        .value_kind:     global_buffer
      - .offset:         56
        .size:           4
        .value_kind:     by_value
      - .offset:         64
        .size:           112
        .value_kind:     by_value
    .group_segment_fixed_size: 83968
    .kernarg_segment_align: 8
    .kernarg_segment_size: 176
    .language:       OpenCL C
    .language_version:
      - 2
      - 0
    .max_flat_workgroup_size: 512
    .name:           _Z11attn_kernelPKtiS0_iS0_iPti6CoArgs
    .private_segment_fixed_size: 0
    .sgpr_count:     74
    .sgpr_spill_count: 0
    .symbol:         _Z11attn_kernelPKtiS0_iS0_iPti6CoArgs.kd
    .uniform_work_group_size: 1
    .uses_dynamic_stack: false
    .vgpr_count:     218
    .vgpr_spill_count: 0
    .wavefront_size: 64
  - .agpr_count:     0
    .args:
      - .offset:         0
        .size:           144
        .value_kind:     by_value
    .group_segment_fixed_size: 77312
    .kernarg_segment_align: 8
    .kernarg_segment_size: 144
    .language:       OpenCL C
    .language_version:
      - 2
      - 0
    .max_flat_workgroup_size: 512
    .name:           _Z12chain_kernelILi0EEv9ChainArgs
    .private_segment_fixed_size: 0
    .sgpr_count:     35
    .sgpr_spill_count: 0
    .symbol:         _Z12chain_kernelILi0EEv9ChainArgs.kd
    .uniform_work_group_size: 1
    .uses_dynamic_stack: false
    .vgpr_count:     224
    .vgpr_spill_count: 0
    .wavefront_size: 64
  - .agpr_count:     0
    .args:
      - .offset:         0
        .size:           144
        .value_kind:     by_value
    .group_segment_fixed_size: 77312
    .kernarg_segment_align: 8
    .kernarg_segment_size: 144
    .language:       OpenCL C
    .language_version:
      - 2
      - 0
    .max_flat_workgroup_size: 512
    .name:           _Z12chain_kernelILi1EEv9ChainArgs
    .private_segment_fixed_size: 0
    .sgpr_count:     35
    .sgpr_spill_count: 0
    .symbol:         _Z12chain_kernelILi1EEv9ChainArgs.kd
    .uniform_work_group_size: 1
    .uses_dynamic_stack: false
    .vgpr_count:     210
    .vgpr_spill_count: 0
    .wavefront_size: 64
